# baseline (speedup 1.0000x reference)
.LBB1_6:
	s_lshr_b32 s55, s2, 8
	s_cmp_eq_u32 s55, 1
	s_cbranch_scc0 .Lskew_done
	s_sleep 64
